# baseline (speedup 1.0000x reference)
_Z12scan2_kernelPKDF16_S0_S0_S0_S0_PKfS2_S2_S2_PDF16_PfS4_:
	s_and_b32 s3, s2, 7
	s_lshr_b32 s2, s2, 3
	s_lshl_b32 s3, s3, 5
	s_or_b32 s2, s2, s3
	s_load_dwordx8 s[4:11], s[0:1], 0x0
	s_load_dwordx8 s[12:19], s[0:1], 0x20
	s_load_dwordx4 s[20:23], s[0:1], 0x40
	s_load_dwordx2 s[24:25], s[0:1], 0x50
	s_and_b32 s26, s2, 3
	s_bfe_u32 s27, s2, 0x50002
	s_lshr_b32 s28, s2, 7
	s_lshl_b32 s29, s26, 3
	v_lshrrev_b32_e32 v1, 6, v0
	v_and_b32_e32 v2, 15, v0
	v_bfe_u32 v3, v0, 4, 2
	v_and_b32_e32 v42, 63, v0
	v_readfirstlane_b32 s40, v1
	v_mov_b32_e32 v43, v0
	v_lshrrev_b32_e32 v14, 4, v43
	v_and_b32_e32 v15, 15, v43
	v_and_b32_e32 v188, 15, v14
	v_xor_b32_e32 v15, v15, v188
	v_lshlrev_b32_e32 v15, 4, v15
	v_lshl_or_b32 v4, v14, 13, v15
	v_lshl_or_b32 v6, v14, 8, v15
	v_lshrrev_b32_e32 v14, 3, v43
	v_and_b32_e32 v15, 7, v43
	v_and_b32_e32 v188, 7, v14
	v_xor_b32_e32 v15, v15, v188
	v_lshlrev_b32_e32 v15, 4, v15
	v_lshl_or_b32 v8, v14, 12, v15
	v_lshlrev_b32_e32 v40, 4, v43
	v_add_u32_e32 v32, 0xc800, v40
	v_add_u32_e32 v43, 0x200, v0
	v_lshrrev_b32_e32 v14, 4, v43
	v_and_b32_e32 v15, 15, v43
	v_and_b32_e32 v188, 15, v14
	v_xor_b32_e32 v15, v15, v188
	v_lshlrev_b32_e32 v15, 4, v15
	v_lshl_or_b32 v5, v14, 13, v15
	v_lshl_or_b32 v7, v14, 8, v15
	v_lshrrev_b32_e32 v14, 3, v43
	v_and_b32_e32 v15, 7, v43
	v_and_b32_e32 v188, 7, v14
	v_xor_b32_e32 v15, v15, v188
	v_lshlrev_b32_e32 v15, 4, v15
	v_lshl_or_b32 v9, v14, 12, v15
	v_lshlrev_b32_e32 v41, 4, v43
	v_add_u32_e32 v33, 0xc800, v41
	s_sub_u32 s45, 11, s40
	s_cmp_lt_u32 s40, 4
	s_cselect_b32 s41, s40, s45
	s_lshr_b32 s42, s41, 1
	s_lshl_b32 s43, s40, 10
	s_lshl_b32 s44, s40, 8
	s_and_b32 s45, s40, 1
	s_lshl_b32 s45, s45, 8
	v_lshl_add_u32 v10, v42, 2, s45
	s_lshl_b32 s45, s41, 4
	v_add_u32_e32 v14, s45, v2
	v_add_u32_e32 v15, 0, v3
	v_xor_b32_e32 v15, v15, v2
	v_lshlrev_b32_e32 v15, 4, v15
	v_lshl_or_b32 v16, v2, 8, v15
	v_add_u32_e32 v20, 0xc800, v16
	v_add_u32_e32 v15, 4, v3
	v_xor_b32_e32 v15, v15, v2
	v_lshlrev_b32_e32 v15, 4, v15
	v_lshl_or_b32 v17, v2, 8, v15
	v_add_u32_e32 v21, 0xc800, v17
	v_add_u32_e32 v15, 8, v3
	v_xor_b32_e32 v15, v15, v2
	v_lshlrev_b32_e32 v15, 4, v15
	v_lshl_or_b32 v18, v2, 8, v15
	v_add_u32_e32 v22, 0xc800, v18
	v_add_u32_e32 v15, 12, v3
	v_xor_b32_e32 v15, v15, v2
	v_lshlrev_b32_e32 v15, 4, v15
	v_lshl_or_b32 v19, v2, 8, v15
	v_add_u32_e32 v23, 0xc800, v19
	v_lshrrev_b32_e32 v188, 1, v3
	v_and_b32_e32 v189, 7, v14
	v_and_b32_e32 v190, 1, v3
	v_lshlrev_b32_e32 v190, 3, v190
	v_lshl_or_b32 v190, v14, 7, v190
	v_add_u32_e32 v15, 0, v188
	v_xor_b32_e32 v15, v15, v189
	v_lshl_add_u32 v24, v15, 4, v190
	v_add_u32_e32 v28, 0xc800, v24
	v_add_u32_e32 v15, 2, v188
	v_xor_b32_e32 v15, v15, v189
	v_lshl_add_u32 v25, v15, 4, v190
	v_add_u32_e32 v29, 0xc800, v25
	v_add_u32_e32 v15, 4, v188
	v_xor_b32_e32 v15, v15, v189
	v_lshl_add_u32 v26, v15, 4, v190
	v_add_u32_e32 v30, 0xc800, v26
	v_add_u32_e32 v15, 6, v188
	v_xor_b32_e32 v15, v15, v189
	v_lshl_add_u32 v27, v15, 4, v190
	v_add_u32_e32 v31, 0xc800, v27
	v_lshlrev_b32_e32 v242, 12, v14
	v_lshl_add_u32 v242, v3, 3, v242
	v_lshlrev_b32_e32 v36, 2, v14
	v_add_u32_e32 v37, 0xc800, v36
	v_lshlrev_b32_e32 v38, 5, v3
	v_add_u32_e32 v39, 0xc800, v38
	s_and_b32 s45, s41, 1
	s_lshl_b32 s45, s45, 4
	v_add_u32_e32 v43, s45, v2
	v_lshlrev_b32_e32 v189, 3, v3
	v_sub_u32_e32 v43, v43, v189
	v_cmp_le_i32_e64 s[52:53], 0, v43
	v_cmp_le_i32_e64 s[54:55], 1, v43
	v_cmp_le_i32_e64 s[56:57], 2, v43
	v_cmp_le_i32_e64 s[58:59], 3, v43
	v_cmp_le_i32_e64 s[60:61], 4, v43
	v_cmp_le_i32_e64 s[62:63], 5, v43
	v_cmp_le_i32_e64 s[64:65], 6, v43
	v_cmp_le_i32_e64 s[66:67], 7, v43
	v_cmp_eq_u32_e32 vcc, 0, v43
	s_nop 1
	v_cndmask_b32_e64 v188, 0, 1.0, vcc
	v_cmp_eq_u32_e32 vcc, 1, v43
	s_nop 1
	v_cndmask_b32_e64 v189, 0, 1.0, vcc
	v_cmp_eq_u32_e32 vcc, 2, v43
	s_nop 1
	v_cndmask_b32_e64 v190, 0, 1.0, vcc
	v_cmp_eq_u32_e32 vcc, 3, v43
	s_nop 1
	v_cndmask_b32_e64 v191, 0, 1.0, vcc
	v_cmp_eq_u32_e32 vcc, 4, v43
	s_nop 1
	v_cndmask_b32_e64 v192, 0, 1.0, vcc
	v_cmp_eq_u32_e32 vcc, 5, v43
	s_nop 1
	v_cndmask_b32_e64 v193, 0, 1.0, vcc
	v_cmp_eq_u32_e32 vcc, 6, v43
	s_nop 1
	v_cndmask_b32_e64 v194, 0, 1.0, vcc
	v_cmp_eq_u32_e32 vcc, 7, v43
	s_nop 1
	v_cndmask_b32_e64 v195, 0, 1.0, vcc
	v_cvt_pk_f16_f32 v92, v188, v189
	v_cvt_pk_f16_f32 v93, v190, v191
	v_cvt_pk_f16_f32 v94, v192, v193
	v_cvt_pk_f16_f32 v95, v194, v195
	v_mov_b32_e32 v250, 0
	v_mov_b32_e32 v251, 0
	v_mov_b32_e32 v188, 0xffff
	v_mov_b32_e32 v189, 0xffff0000
	v_cndmask_b32_e64 v190, 0, v188, s[52:53]
	v_cndmask_b32_e64 v191, 0, v189, s[54:55]
	v_or_b32_e32 v244, v190, v191
	v_cndmask_b32_e64 v190, 0, v188, s[56:57]
	v_cndmask_b32_e64 v191, 0, v189, s[58:59]
	v_or_b32_e32 v245, v190, v191
	v_cndmask_b32_e64 v190, 0, v188, s[60:61]
	v_cndmask_b32_e64 v191, 0, v189, s[62:63]
	v_or_b32_e32 v246, v190, v191
	v_cndmask_b32_e64 v190, 0, v188, s[64:65]
	v_cndmask_b32_e64 v191, 0, v189, s[66:67]
	v_or_b32_e32 v247, v190, v191
	s_waitcnt lgkmcnt(0)
	s_lshl_b32 s45, s28, 12
	s_lshl_b32 s48, s27, 7
	s_add_u32 s45, s45, s48
	s_lshl_b32 s48, s45, 9
	s_add_u32 s48, s4, s48
	s_addc_u32 s49, s5, 0
	v_lshlrev_b32_e32 v188, 9, v14
	v_lshl_add_u32 v188, v3, 4, v188
	global_load_dwordx4 v[44:47], v188, s[48:49] offset:256
	global_load_dwordx4 v[48:51], v188, s[48:49] offset:320
	global_load_dwordx4 v[52:55], v188, s[48:49] offset:384
	global_load_dwordx4 v[56:59], v188, s[48:49] offset:448
	s_lshl_b32 s48, s28, 5
	s_add_u32 s48, s48, s27
	s_lshl_b32 s48, s48, 15
	s_add_u32 s48, s10, s48
	s_addc_u32 s49, s11, 0
	v_lshlrev_b32_e32 v188, 8, v14
	v_lshl_add_u32 v188, v3, 4, v188
	global_load_dwordx4 v[144:147], v188, s[48:49] offset:0
	global_load_dwordx4 v[148:151], v188, s[48:49] offset:64
	global_load_dwordx4 v[152:155], v188, s[48:49] offset:128
	global_load_dwordx4 v[156:159], v188, s[48:49] offset:192
	v_and_b32_e32 v188, 7, v42
	v_add_u32_e32 v188, s29, v188
	v_lshlrev_b32_e32 v188, 2, v188
	global_load_dword v11, v188, s[20:21]
	global_load_dword v12, v188, s[18:19]
	s_mul_i32 s48, s28, 0x900
	s_lshl_b32 s49, s29, 6
	s_add_u32 s48, s48, s49
	s_lshl_b32 s48, s48, 13
	s_lshl_b32 s49, s27, 8
	s_add_u32 s48, s48, s49
	s_add_u32 s30, s6, s48
	s_addc_u32 s31, s7, 0
	s_lshl_b32 s48, s28, 5
	s_add_u32 s48, s48, s27
	s_lshl_b32 s48, s48, 5
	s_add_u32 s48, s48, s29
	s_lshl_b32 s48, s48, 14
	s_add_u32 s32, s12, s48
	s_addc_u32 s33, s13, 0
	s_lshl_b32 s48, s45, 12
	s_lshl_b32 s49, s29, 7
	s_add_u32 s48, s48, s49
	s_add_u32 s34, s8, s48
	s_addc_u32 s35, s9, 0
	s_add_u32 s38, s22, s48
	s_addc_u32 s39, s23, 0
	s_lshl_b32 s48, s28, 5
	s_add_u32 s48, s48, s29
	s_lshl_b32 s48, s48, 14
	s_lshl_b32 s49, s27, 9
	s_add_u32 s48, s48, s49
	s_lshr_b32 s49, s40, 1
	s_cmp_eq_u32 s49, 1
	s_cselect_b32 s50, s14, s16
	s_cselect_b32 s51, s15, s17
	s_add_u32 s36, s50, s48
	s_addc_u32 s37, s51, 0
	s_lshl_b32 s48, s45, 2
	s_add_u32 s24, s24, s48
	s_addc_u32 s25, s25, 0
	v_lshlrev_b32_e32 v15, 2, v14
	s_mov_b32 s51, 0xbfb8aa3b
	s_mov_b32 s50, 0x41800000
	s_add_u32 m0, s43, 0x0
	s_nop 0
	global_load_lds_dwordx4 v4, s[30:31]
	s_add_u32 m0, s43, 0x4000
	s_nop 0
	global_load_lds_dwordx4 v6, s[32:33]
	s_add_u32 m0, s43, 0x8000
	s_nop 0
	global_load_lds_dwordx4 v8, s[34:35]
	s_add_u32 m0, s43, 0x2000
	s_nop 0
	global_load_lds_dwordx4 v5, s[30:31]
	s_add_u32 m0, s43, 0x6000
	s_nop 0
	global_load_lds_dwordx4 v7, s[32:33]
	s_add_u32 m0, s43, 0xa000
	s_nop 0
	global_load_lds_dwordx4 v9, s[34:35]
	s_add_u32 m0, s44, 0xc000
	s_nop 0
	global_load_lds_dword v10, s[36:37]
	s_add_u32 s30, s30, 0x80000
	s_addc_u32 s31, s31, 0
	s_add_u32 s32, s32, 0x4000
	s_addc_u32 s33, s33, 0
	s_add_u32 s34, s34, 0x80
	s_addc_u32 s35, s35, 0
	s_add_u32 s36, s36, 0x4000
	s_addc_u32 s37, s37, 0
	global_load_dword v243, v10, s[36:37]
	global_load_dword v243, v10, s[36:37]
	global_load_dword v243, v10, s[36:37]
	global_load_dword v243, v10, s[36:37]
	s_waitcnt vmcnt(16)
	v_cvt_f32_f16_e32 v60, v144
	v_cvt_f32_f16_sdwa v61, v144 dst_sel:DWORD dst_unused:UNUSED_PAD src0_sel:WORD_1
	v_cvt_f32_f16_e32 v62, v145
	v_cvt_f32_f16_sdwa v63, v145 dst_sel:DWORD dst_unused:UNUSED_PAD src0_sel:WORD_1
	v_cvt_f32_f16_e32 v64, v146
	v_cvt_f32_f16_sdwa v65, v146 dst_sel:DWORD dst_unused:UNUSED_PAD src0_sel:WORD_1
	v_cvt_f32_f16_e32 v66, v147
	v_cvt_f32_f16_sdwa v67, v147 dst_sel:DWORD dst_unused:UNUSED_PAD src0_sel:WORD_1
	s_waitcnt vmcnt(15)
	v_cvt_f32_f16_e32 v68, v148
	v_cvt_f32_f16_sdwa v69, v148 dst_sel:DWORD dst_unused:UNUSED_PAD src0_sel:WORD_1
	v_cvt_f32_f16_e32 v70, v149
	v_cvt_f32_f16_sdwa v71, v149 dst_sel:DWORD dst_unused:UNUSED_PAD src0_sel:WORD_1
	v_cvt_f32_f16_e32 v72, v150
	v_cvt_f32_f16_sdwa v73, v150 dst_sel:DWORD dst_unused:UNUSED_PAD src0_sel:WORD_1
	v_cvt_f32_f16_e32 v74, v151
	v_cvt_f32_f16_sdwa v75, v151 dst_sel:DWORD dst_unused:UNUSED_PAD src0_sel:WORD_1
	s_waitcnt vmcnt(14)
	v_cvt_f32_f16_e32 v76, v152
	v_cvt_f32_f16_sdwa v77, v152 dst_sel:DWORD dst_unused:UNUSED_PAD src0_sel:WORD_1
	v_cvt_f32_f16_e32 v78, v153
	v_cvt_f32_f16_sdwa v79, v153 dst_sel:DWORD dst_unused:UNUSED_PAD src0_sel:WORD_1
	v_cvt_f32_f16_e32 v80, v154
	v_cvt_f32_f16_sdwa v81, v154 dst_sel:DWORD dst_unused:UNUSED_PAD src0_sel:WORD_1
	v_cvt_f32_f16_e32 v82, v155
	v_cvt_f32_f16_sdwa v83, v155 dst_sel:DWORD dst_unused:UNUSED_PAD src0_sel:WORD_1
	s_waitcnt vmcnt(13)
	v_cvt_f32_f16_e32 v84, v156
	v_cvt_f32_f16_sdwa v85, v156 dst_sel:DWORD dst_unused:UNUSED_PAD src0_sel:WORD_1
	v_cvt_f32_f16_e32 v86, v157
	v_cvt_f32_f16_sdwa v87, v157 dst_sel:DWORD dst_unused:UNUSED_PAD src0_sel:WORD_1
	v_cvt_f32_f16_e32 v88, v158
	v_cvt_f32_f16_sdwa v89, v158 dst_sel:DWORD dst_unused:UNUSED_PAD src0_sel:WORD_1
	v_cvt_f32_f16_e32 v90, v159
	v_cvt_f32_f16_sdwa v91, v159 dst_sel:DWORD dst_unused:UNUSED_PAD src0_sel:WORD_1
	s_waitcnt vmcnt(11)
	s_waitcnt vmcnt(12)
	v_mul_f32_e32 v11, 0x41800000, v11
	v_mov_b32_e32 v212, v16
	v_mov_b32_e32 v216, v24
	v_mov_b32_e32 v213, v17
	v_mov_b32_e32 v217, v25
	v_mov_b32_e32 v214, v18
	v_mov_b32_e32 v218, v26
	v_mov_b32_e32 v215, v19
	v_mov_b32_e32 v219, v27
	v_mov_b32_e32 v220, v36
	v_mov_b32_e32 v221, v38
	s_mov_b32 s70, 0xc800
	s_mov_b32 s71, 0xc800
	s_mov_b32 s48, 0

.Lmy_s2_diag5:
	ds_read_b64 v[234:235], v216 offset:32768
	ds_read_b64 v[236:237], v217 offset:32768
	ds_read_b64 v[238:239], v218 offset:32768
	ds_read_b64 v[240:241], v219 offset:32768
	s_waitcnt lgkmcnt(4)
	v_fma_f32 v188, v188, s51, v189
	v_exp_f32_e32 v188, v188
	s_nop 0
	v_pk_mul_f32 v[176:177], v[176:177], v[188:189] op_sel_hi:[1,0]
	v_pk_mul_f32 v[178:179], v[178:179], v[188:189] op_sel_hi:[1,0]
	v_pk_mul_f32 v[180:181], v[180:181], v[188:189] op_sel_hi:[1,0]
	v_pk_mul_f32 v[182:183], v[182:183], v[188:189] op_sel_hi:[1,0]
	v_pk_mul_f32 v[176:177], v[60:61], v[176:177]
	v_pk_mul_f32 v[178:179], v[62:63], v[178:179]
	v_pk_mul_f32 v[180:181], v[64:65], v[180:181]
	v_pk_mul_f32 v[182:183], v[66:67], v[182:183]
	v_cvt_pk_f16_f32 v184, v176, v177
	v_cvt_pk_f16_f32 v185, v178, v179
	v_cvt_pk_f16_f32 v186, v180, v181
	v_cvt_pk_f16_f32 v187, v182, v183
	v_and_b32_e32 v184, v244, v184
	v_and_b32_e32 v185, v245, v185
	v_and_b32_e32 v186, v246, v186
	v_and_b32_e32 v187, v247, v187
	s_nop 1
	v_mfma_f32_16x16x32_f16 v[112:115], v[144:147], v[184:187], 0
	v_mfma_f32_16x16x32_f16 v[116:119], v[148:151], v[184:187], 0
	v_mfma_f32_16x16x32_f16 v[120:123], v[152:155], v[184:187], 0
	v_mfma_f32_16x16x32_f16 v[124:127], v[156:159], v[184:187], 0
	v_mfma_f32_16x16x32_f16 v[128:131], v[144:147], v[92:95], 0
	v_mfma_f32_16x16x32_f16 v[132:135], v[148:151], v[92:95], 0
	v_mfma_f32_16x16x32_f16 v[136:139], v[152:155], v[92:95], 0
	v_mfma_f32_16x16x32_f16 v[140:143], v[156:159], v[92:95], 0
	s_branch .Lmy_s2_kend4

.Lmy_s2_diag7:
	ds_read_b64 v[234:235], v216 offset:32768
	ds_read_b64 v[236:237], v217 offset:32768
	ds_read_b64 v[238:239], v218 offset:32768
	ds_read_b64 v[240:241], v219 offset:32768
	s_waitcnt lgkmcnt(4)
	v_fma_f32 v232, v232, s51, v189
	v_exp_f32_e32 v232, v232
	s_nop 0
	v_pk_mul_f32 v[224:225], v[224:225], v[232:233] op_sel_hi:[1,0]
	v_pk_mul_f32 v[226:227], v[226:227], v[232:233] op_sel_hi:[1,0]
	v_pk_mul_f32 v[228:229], v[228:229], v[232:233] op_sel_hi:[1,0]
	v_pk_mul_f32 v[230:231], v[230:231], v[232:233] op_sel_hi:[1,0]
	v_pk_mul_f32 v[224:225], v[68:69], v[224:225]
	v_pk_mul_f32 v[226:227], v[70:71], v[226:227]
	v_pk_mul_f32 v[228:229], v[72:73], v[228:229]
	v_pk_mul_f32 v[230:231], v[74:75], v[230:231]
	v_cvt_pk_f16_f32 v184, v224, v225
	v_cvt_pk_f16_f32 v185, v226, v227
	v_cvt_pk_f16_f32 v186, v228, v229
	v_cvt_pk_f16_f32 v187, v230, v231
	v_and_b32_e32 v184, v244, v184
	v_and_b32_e32 v185, v245, v185
	v_and_b32_e32 v186, v246, v186
	v_and_b32_e32 v187, v247, v187
	s_nop 1
	v_mfma_f32_16x16x32_f16 v[112:115], v[160:163], v[184:187], v[112:115]
	v_mfma_f32_16x16x32_f16 v[116:119], v[164:167], v[184:187], v[116:119]
	v_mfma_f32_16x16x32_f16 v[120:123], v[168:171], v[184:187], v[120:123]
	v_mfma_f32_16x16x32_f16 v[124:127], v[172:175], v[184:187], v[124:127]
	v_mfma_f32_16x16x32_f16 v[128:131], v[160:163], v[92:95], 0
	v_mfma_f32_16x16x32_f16 v[132:135], v[164:167], v[92:95], 0
	v_mfma_f32_16x16x32_f16 v[136:139], v[168:171], v[92:95], 0
	v_mfma_f32_16x16x32_f16 v[140:143], v[172:175], v[92:95], 0
	s_branch .Lmy_s2_kend4

.Lmy_s2_diag9:
	ds_read_b64 v[234:235], v216 offset:32768
	ds_read_b64 v[236:237], v217 offset:32768
	ds_read_b64 v[238:239], v218 offset:32768
	ds_read_b64 v[240:241], v219 offset:32768
	s_waitcnt lgkmcnt(4)
	v_fma_f32 v188, v188, s51, v189
	v_exp_f32_e32 v188, v188
	s_nop 0
	v_pk_mul_f32 v[176:177], v[176:177], v[188:189] op_sel_hi:[1,0]
	v_pk_mul_f32 v[178:179], v[178:179], v[188:189] op_sel_hi:[1,0]
	v_pk_mul_f32 v[180:181], v[180:181], v[188:189] op_sel_hi:[1,0]
	v_pk_mul_f32 v[182:183], v[182:183], v[188:189] op_sel_hi:[1,0]
	v_pk_mul_f32 v[176:177], v[76:77], v[176:177]
	v_pk_mul_f32 v[178:179], v[78:79], v[178:179]
	v_pk_mul_f32 v[180:181], v[80:81], v[180:181]
	v_pk_mul_f32 v[182:183], v[82:83], v[182:183]
	v_cvt_pk_f16_f32 v184, v176, v177
	v_cvt_pk_f16_f32 v185, v178, v179
	v_cvt_pk_f16_f32 v186, v180, v181
	v_cvt_pk_f16_f32 v187, v182, v183
	v_and_b32_e32 v184, v244, v184
	v_and_b32_e32 v185, v245, v185
	v_and_b32_e32 v186, v246, v186
	v_and_b32_e32 v187, v247, v187
	s_nop 1
	v_mfma_f32_16x16x32_f16 v[112:115], v[144:147], v[184:187], v[112:115]
	v_mfma_f32_16x16x32_f16 v[116:119], v[148:151], v[184:187], v[116:119]
	v_mfma_f32_16x16x32_f16 v[120:123], v[152:155], v[184:187], v[120:123]
	v_mfma_f32_16x16x32_f16 v[124:127], v[156:159], v[184:187], v[124:127]
	v_mfma_f32_16x16x32_f16 v[128:131], v[144:147], v[92:95], 0
	v_mfma_f32_16x16x32_f16 v[132:135], v[148:151], v[92:95], 0
	v_mfma_f32_16x16x32_f16 v[136:139], v[152:155], v[92:95], 0
	v_mfma_f32_16x16x32_f16 v[140:143], v[156:159], v[92:95], 0
	s_branch .Lmy_s2_kend4

.Lmy_s2_diag11:
	ds_read_b64 v[234:235], v216 offset:32768
	ds_read_b64 v[236:237], v217 offset:32768
	ds_read_b64 v[238:239], v218 offset:32768
	ds_read_b64 v[240:241], v219 offset:32768
	s_waitcnt lgkmcnt(4)
	v_fma_f32 v232, v232, s51, v189
	v_exp_f32_e32 v232, v232
	s_nop 0
	v_pk_mul_f32 v[224:225], v[224:225], v[232:233] op_sel_hi:[1,0]
	v_pk_mul_f32 v[226:227], v[226:227], v[232:233] op_sel_hi:[1,0]
	v_pk_mul_f32 v[228:229], v[228:229], v[232:233] op_sel_hi:[1,0]
	v_pk_mul_f32 v[230:231], v[230:231], v[232:233] op_sel_hi:[1,0]
	v_pk_mul_f32 v[224:225], v[84:85], v[224:225]
	v_pk_mul_f32 v[226:227], v[86:87], v[226:227]
	v_pk_mul_f32 v[228:229], v[88:89], v[228:229]
	v_pk_mul_f32 v[230:231], v[90:91], v[230:231]
	v_cvt_pk_f16_f32 v184, v224, v225
	v_cvt_pk_f16_f32 v185, v226, v227
	v_cvt_pk_f16_f32 v186, v228, v229
	v_cvt_pk_f16_f32 v187, v230, v231
	v_and_b32_e32 v184, v244, v184
	v_and_b32_e32 v185, v245, v185
	v_and_b32_e32 v186, v246, v186
	v_and_b32_e32 v187, v247, v187
	s_nop 1
	v_mfma_f32_16x16x32_f16 v[112:115], v[160:163], v[184:187], v[112:115]
	v_mfma_f32_16x16x32_f16 v[116:119], v[164:167], v[184:187], v[116:119]
	v_mfma_f32_16x16x32_f16 v[120:123], v[168:171], v[184:187], v[120:123]
	v_mfma_f32_16x16x32_f16 v[124:127], v[172:175], v[184:187], v[124:127]
	v_mfma_f32_16x16x32_f16 v[128:131], v[160:163], v[92:95], 0
	v_mfma_f32_16x16x32_f16 v[132:135], v[164:167], v[92:95], 0
	v_mfma_f32_16x16x32_f16 v[136:139], v[168:171], v[92:95], 0
	v_mfma_f32_16x16x32_f16 v[140:143], v[172:175], v[92:95], 0
	s_branch .Lmy_s2_kend4
